# v28 + final phase: loop-invariant final-norm gain fragments loaded once instead of 8 dependent load/store round trips per token
# speedup vs baseline: 1.0054x; 1.0054x over previous
; __device__ __forceinline__ void p14_final(Frame& F) {
;     const int gw = F.bid * NWAVES + F.wave, NGW = F.G * NWAVES, lane = F.lane;
;     const float* gf = WSP(float, WS_MODV) + 5 * 2048;
;     const unsigned lb1 = (unsigned)lane * 16u, lb4 = (unsigned)lane * 64u;
;     const int shbase = __builtin_amdgcn_readfirstlane(WSP(int, WS_TILEE)[NEXP]) * 256;
;     const unsigned char* ys = WSP(unsigned char, WS_YS);
;     for (int t0 = gw; t0 < S_; t0 += NGW) {
;         const int t = __builtin_amdgcn_readfirstlane(t0);
;         float acc[32];
; #pragma unroll
;         for (int i = 0; i < 32; ++i) acc[i] = 0.f;
;         const int* so = WSP(int, WS_SDST) + (size_t)t * 8;
;     ...
;             for (int q = 0; q < 4; ++q) { const f32x4 g0 = ldf16(INF(I_FNG) + 1024 * j + 4 * q, lb4); f32x4 o0;
.LBB0_1762:
	s_cmp_lt_i32 s28, 16
	s_cselect_b64 s[6:7], -1, 0
	s_and_b64 s[4:5], s[6:7], s[4:5]
	s_andn2_b64 vcc, exec, s[4:5]
	s_cbranch_vccnz .LBB0_1768
	s_load_dwordx2 s[4:5], s[0:1], 0xc8
	s_waitcnt vmcnt(0)
	v_mov_b32_e32 v1, 0x160000
	v_readfirstlane_b32 s3, v0
	s_ashr_i32 s3, s3, 6
	s_lshl_b32 s2, s2, 3
	s_waitcnt lgkmcnt(0)
	global_load_dword v1, v1, s[4:5] offset:256
	s_add_i32 s2, s3, s2
	s_cmpk_gt_i32 s2, 0x3fff
	s_waitcnt vmcnt(0)
	v_readfirstlane_b32 s3, v1
	s_cbranch_scc1 .LBB0_1768
	v_mbcnt_lo_u32_b32 v10, -1, 0
	v_mbcnt_hi_u32_b32 v10, -1, v10
	v_and_b32_e32 v11, 64, v10
	v_add_u32_e32 v11, 64, v11
	v_xor_b32_e32 v12, 1, v10
	v_cmp_lt_i32_e32 vcc, v12, v11
	v_and_b32_e32 v1, 63, v0
	v_lshlrev_b32_e32 v4, 4, v1
	v_cndmask_b32_e32 v12, v10, v12, vcc
	v_lshlrev_b32_e32 v58, 2, v12
	v_xor_b32_e32 v12, 2, v10
	v_cmp_lt_i32_e32 vcc, v12, v11
	v_mov_b32_e32 v5, 0
	v_lshlrev_b32_e32 v0, 6, v1
	v_cndmask_b32_e32 v12, v10, v12, vcc
	v_lshlrev_b32_e32 v59, 2, v12
	v_xor_b32_e32 v12, 4, v10
	v_cmp_lt_i32_e32 vcc, v12, v11
	v_lshl_add_u64 v[2:3], s[4:5], 0, v[4:5]
	s_mov_b64 s[8:9], 0xb200000
	v_cndmask_b32_e32 v12, v10, v12, vcc
	v_lshlrev_b32_e32 v60, 2, v12
	v_xor_b32_e32 v12, 8, v10
	v_cmp_lt_i32_e32 vcc, v12, v11
	v_lshlrev_b32_e32 v4, 5, v1
	v_mov_b32_e32 v1, v5
	v_cndmask_b32_e32 v12, v10, v12, vcc
	v_lshl_add_u64 v[6:7], v[2:3], 0, s[8:9]
	v_lshl_add_u64 v[2:3], s[4:5], 0, v[0:1]
	s_mov_b64 s[8:9], 0x10a000
	v_lshlrev_b32_e32 v61, 2, v12
	v_xor_b32_e32 v12, 16, v10
	v_lshl_add_u64 v[8:9], v[2:3], 0, s[8:9]
	v_cmp_lt_i32_e32 vcc, v12, v11
	s_load_dwordx4 s[8:11], s[0:1], 0xb8
	s_mov_b64 s[0:1], 0x10b000
	v_cndmask_b32_e32 v12, v10, v12, vcc
	v_lshlrev_b32_e32 v62, 2, v12
	v_xor_b32_e32 v12, 32, v10
	v_cmp_lt_i32_e32 vcc, v12, v11
	s_waitcnt lgkmcnt(0)
	v_lshl_add_u64 v[14:15], s[8:9], 0, v[0:1]
	s_lshl_b32 s7, s3, 8
	v_cndmask_b32_e32 v10, v10, v12, vcc
	v_lshlrev_b32_e32 v63, 2, v10
	v_lshl_add_u64 v[10:11], v[2:3], 0, s[0:1]
	s_mov_b64 s[0:1], 0x1000
	v_lshl_add_u64 v[16:17], v[14:15], 0, s[0:1]
	s_mov_b64 s[0:1], 0x1010
	v_lshl_add_u64 v[18:19], v[14:15], 0, s[0:1]
	s_mov_b64 s[0:1], 0x1020
	v_lshl_add_u64 v[20:21], v[14:15], 0, s[0:1]
	s_mov_b64 s[0:1], 0x1030
	v_lshl_add_u64 v[12:13], s[10:11], 0, v[0:1]
	v_lshl_add_u64 v[22:23], v[14:15], 0, s[0:1]
	v_lshl_add_u64 v[0:1], s[4:5], 0, v[4:5]
	s_mov_b64 s[0:1], 0x27700000
	v_lshl_add_u64 v[24:25], v[0:1], 0, s[0:1]
	v_mov_b32_e32 v4, 0x1000000
	s_mov_b32 s6, 0x3d800000
	v_mov_b32_e32 v64, 0x358637bd
	s_mov_b32 s12, 0xf800000
	v_mov_b32_e32 v65, 0x260
	s_movk_i32 s13, 0x1000
	global_load_dwordx4 v[192:195], v[14:15], off
	global_load_dwordx4 v[196:199], v[14:15], off offset:16
	global_load_dwordx4 v[200:203], v[14:15], off offset:32
	global_load_dwordx4 v[204:207], v[14:15], off offset:48
	global_load_dwordx4 v[208:211], v[16:17], off
	global_load_dwordx4 v[212:215], v[18:19], off
	global_load_dwordx4 v[216:219], v[20:21], off
	global_load_dwordx4 v[220:223], v[22:23], off
	s_waitcnt vmcnt(0)

; __device__ __forceinline__ void acc_fp8x16(float* a, u32x4 w) {
; #pragma unroll
;     for (int i = 0; i < 4; ++i) { const f32x2_ lo = __builtin_amdgcn_cvt_pk_f32_fp8((int)w[i], false), hi = __builtin_amdgcn_cvt_pk_f32_fp8((int)w[i], true);
;         a[4 * i] += lo.x; a[4 * i + 1] += lo.y; a[4 * i + 2] += hi.x; a[4 * i + 3] += hi.y; }
; }
; __device__ __forceinline__ void p14_final(Frame& F) {
;     const int gw = F.bid * NWAVES + F.wave, NGW = F.G * NWAVES, lane = F.lane;
;     const float* gf = WSP(float, WS_MODV) + 5 * 2048;
;     const unsigned lb1 = (unsigned)lane * 16u, lb4 = (unsigned)lane * 64u;
;     const int shbase = __builtin_amdgcn_readfirstlane(WSP(int, WS_TILEE)[NEXP]) * 256;
;     const unsigned char* ys = WSP(unsigned char, WS_YS);
;     for (int t0 = gw; t0 < S_; t0 += NGW) {
;         const int t = __builtin_amdgcn_readfirstlane(t0);
;         float acc[32];
; #pragma unroll
;         for (int i = 0; i < 32; ++i) acc[i] = 0.f;
;         const int* so = WSP(int, WS_SDST) + (size_t)t * 8;
; #pragma unroll 4
;         for (int k = 0; k < 8; ++k) { const unsigned char* yr = ys + (size_t)__builtin_amdgcn_readfirstlane(so[k]) * DM;
; #pragma unroll
;             for (int j = 0; j < 2; ++j) acc_fp8x16(acc + 16 * j, ldu16(yr + 1024 * j, lb1)); }
.LBB0_1766:
	s_add_u32 s8, s14, s0
	s_addc_u32 s9, s15, s1
	global_load_dwordx4 v[0:3], v4, s[8:9]
	s_waitcnt vmcnt(0)
	v_readfirstlane_b32 s8, v0
	v_readfirstlane_b32 s10, v1
	v_readfirstlane_b32 s16, v2
	v_readfirstlane_b32 s18, v3
	s_ashr_i32 s9, s8, 31
	s_ashr_i32 s11, s10, 31
	s_ashr_i32 s17, s16, 31
	s_ashr_i32 s19, s18, 31
	s_lshl_b64 s[8:9], s[8:9], 11
	s_lshl_b64 s[10:11], s[10:11], 11
	s_lshl_b64 s[16:17], s[16:17], 11
	s_lshl_b64 s[18:19], s[18:19], 11
	v_lshl_add_u64 v[94:95], v[6:7], 0, s[8:9]
	v_lshl_add_u64 v[96:97], v[6:7], 0, s[10:11]
	v_lshl_add_u64 v[98:99], v[6:7], 0, s[16:17]
	v_lshl_add_u64 v[100:101], v[6:7], 0, s[18:19]
	global_load_dwordx4 v[0:3], v[94:95], off
	global_load_dwordx4 v[66:69], v[94:95], off offset:1024
	global_load_dwordx4 v[70:73], v[96:97], off
	global_load_dwordx4 v[74:77], v[96:97], off offset:1024
	global_load_dwordx4 v[78:81], v[98:99], off
	global_load_dwordx4 v[82:85], v[98:99], off offset:1024
	global_load_dwordx4 v[86:89], v[100:101], off
	global_load_dwordx4 v[90:93], v[100:101], off offset:1024
	s_add_u32 s0, s0, 16
	s_addc_u32 s1, s1, 0
	s_cmp_eq_u32 s0, 32
	s_waitcnt vmcnt(7)
	v_cvt_pk_f32_fp8_e32 v[94:95], v0
	v_cvt_pk_f32_fp8_sdwa v[96:97], v0 src0_sel:WORD_1
	v_cvt_pk_f32_fp8_e32 v[98:99], v1
	v_cvt_pk_f32_fp8_sdwa v[0:1], v1 src0_sel:WORD_1
	v_cvt_pk_f32_fp8_e32 v[100:101], v2
	v_cvt_pk_f32_fp8_sdwa v[102:103], v2 src0_sel:WORD_1
	v_cvt_pk_f32_fp8_e32 v[104:105], v3
	v_cvt_pk_f32_fp8_sdwa v[2:3], v3 src0_sel:WORD_1
	s_waitcnt vmcnt(6)
	v_cvt_pk_f32_fp8_e32 v[106:107], v66
	v_cvt_pk_f32_fp8_sdwa v[108:109], v66 src0_sel:WORD_1
	v_cvt_pk_f32_fp8_e32 v[110:111], v67
	v_cvt_pk_f32_fp8_sdwa v[66:67], v67 src0_sel:WORD_1
	v_cvt_pk_f32_fp8_e32 v[112:113], v68
	v_cvt_pk_f32_fp8_sdwa v[114:115], v68 src0_sel:WORD_1
	v_cvt_pk_f32_fp8_e32 v[116:117], v69
	v_cvt_pk_f32_fp8_sdwa v[68:69], v69 src0_sel:WORD_1
	s_waitcnt vmcnt(5)
	v_cvt_pk_f32_fp8_e32 v[118:119], v70
	v_cvt_pk_f32_fp8_sdwa v[120:121], v70 src0_sel:WORD_1
	v_cvt_pk_f32_fp8_e32 v[122:123], v71
	v_cvt_pk_f32_fp8_sdwa v[70:71], v71 src0_sel:WORD_1
	v_cvt_pk_f32_fp8_e32 v[124:125], v72
	v_cvt_pk_f32_fp8_sdwa v[126:127], v72 src0_sel:WORD_1
	v_cvt_pk_f32_fp8_e32 v[128:129], v73
	v_cvt_pk_f32_fp8_sdwa v[72:73], v73 src0_sel:WORD_1
	s_waitcnt vmcnt(4)
	v_cvt_pk_f32_fp8_e32 v[130:131], v74
	v_cvt_pk_f32_fp8_sdwa v[132:133], v74 src0_sel:WORD_1
	v_cvt_pk_f32_fp8_e32 v[134:135], v75
	v_cvt_pk_f32_fp8_sdwa v[74:75], v75 src0_sel:WORD_1
	v_cvt_pk_f32_fp8_e32 v[136:137], v76
	v_cvt_pk_f32_fp8_sdwa v[138:139], v76 src0_sel:WORD_1
	v_cvt_pk_f32_fp8_e32 v[140:141], v77
	v_cvt_pk_f32_fp8_sdwa v[76:77], v77 src0_sel:WORD_1
	s_waitcnt vmcnt(3)
	v_cvt_pk_f32_fp8_e32 v[142:143], v78
	v_cvt_pk_f32_fp8_sdwa v[144:145], v78 src0_sel:WORD_1
	v_cvt_pk_f32_fp8_e32 v[146:147], v79
	v_cvt_pk_f32_fp8_sdwa v[78:79], v79 src0_sel:WORD_1
	v_cvt_pk_f32_fp8_e32 v[148:149], v80
	v_cvt_pk_f32_fp8_sdwa v[150:151], v80 src0_sel:WORD_1
	v_cvt_pk_f32_fp8_e32 v[152:153], v81
	v_cvt_pk_f32_fp8_sdwa v[80:81], v81 src0_sel:WORD_1
	s_waitcnt vmcnt(2)
	v_cvt_pk_f32_fp8_e32 v[154:155], v82
	v_cvt_pk_f32_fp8_sdwa v[156:157], v82 src0_sel:WORD_1
	v_cvt_pk_f32_fp8_e32 v[158:159], v83
	v_cvt_pk_f32_fp8_sdwa v[82:83], v83 src0_sel:WORD_1
	v_cvt_pk_f32_fp8_e32 v[160:161], v84
	v_cvt_pk_f32_fp8_sdwa v[162:163], v84 src0_sel:WORD_1
	v_cvt_pk_f32_fp8_e32 v[164:165], v85
	v_cvt_pk_f32_fp8_sdwa v[84:85], v85 src0_sel:WORD_1
	s_waitcnt vmcnt(1)
	v_cvt_pk_f32_fp8_e32 v[166:167], v86
	v_cvt_pk_f32_fp8_sdwa v[168:169], v86 src0_sel:WORD_1
	v_cvt_pk_f32_fp8_e32 v[170:171], v87
	v_cvt_pk_f32_fp8_sdwa v[86:87], v87 src0_sel:WORD_1
	v_cvt_pk_f32_fp8_e32 v[172:173], v88
	v_cvt_pk_f32_fp8_sdwa v[174:175], v88 src0_sel:WORD_1
	v_cvt_pk_f32_fp8_e32 v[176:177], v89
	v_cvt_pk_f32_fp8_sdwa v[88:89], v89 src0_sel:WORD_1
	s_waitcnt vmcnt(0)
	v_cvt_pk_f32_fp8_e32 v[178:179], v90
	v_cvt_pk_f32_fp8_sdwa v[180:181], v90 src0_sel:WORD_1
	v_cvt_pk_f32_fp8_e32 v[182:183], v91
	v_cvt_pk_f32_fp8_sdwa v[90:91], v91 src0_sel:WORD_1
	v_cvt_pk_f32_fp8_e32 v[184:185], v92
	v_cvt_pk_f32_fp8_sdwa v[186:187], v92 src0_sel:WORD_1
	v_cvt_pk_f32_fp8_e32 v[188:189], v93
	v_cvt_pk_f32_fp8_sdwa v[92:93], v93 src0_sel:WORD_1
	v_pk_add_f32 v[40:41], v[40:41], v[94:95]
	v_pk_add_f32 v[44:45], v[44:45], v[96:97]
	v_pk_add_f32 v[46:47], v[46:47], v[98:99]
	v_pk_add_f32 v[0:1], v[48:49], v[0:1]
	v_pk_add_f32 v[48:49], v[50:51], v[100:101]
	v_pk_add_f32 v[50:51], v[52:53], v[102:103]
	v_pk_add_f32 v[52:53], v[54:55], v[104:105]
	v_pk_add_f32 v[2:3], v[56:57], v[2:3]
	v_pk_add_f32 v[42:43], v[42:43], v[106:107]
	v_pk_add_f32 v[36:37], v[36:37], v[108:109]
	v_pk_add_f32 v[34:35], v[34:35], v[110:111]
	v_pk_add_f32 v[32:33], v[32:33], v[66:67]
	v_pk_add_f32 v[30:31], v[30:31], v[112:113]
	v_pk_add_f32 v[28:29], v[28:29], v[114:115]
	v_pk_add_f32 v[26:27], v[26:27], v[116:117]
	v_pk_add_f32 v[38:39], v[38:39], v[68:69]
	v_pk_add_f32 v[40:41], v[40:41], v[118:119]
	v_pk_add_f32 v[44:45], v[44:45], v[120:121]
	v_pk_add_f32 v[46:47], v[46:47], v[122:123]
	v_pk_add_f32 v[0:1], v[0:1], v[70:71]
	v_pk_add_f32 v[48:49], v[48:49], v[124:125]
	v_pk_add_f32 v[50:51], v[50:51], v[126:127]
	v_pk_add_f32 v[52:53], v[52:53], v[128:129]
	v_pk_add_f32 v[2:3], v[2:3], v[72:73]
	v_pk_add_f32 v[42:43], v[42:43], v[130:131]
	v_pk_add_f32 v[36:37], v[36:37], v[132:133]
	v_pk_add_f32 v[34:35], v[34:35], v[134:135]
	v_pk_add_f32 v[32:33], v[32:33], v[74:75]
	v_pk_add_f32 v[30:31], v[30:31], v[136:137]
	v_pk_add_f32 v[28:29], v[28:29], v[138:139]
	v_pk_add_f32 v[26:27], v[26:27], v[140:141]
	v_pk_add_f32 v[38:39], v[38:39], v[76:77]
	v_pk_add_f32 v[40:41], v[40:41], v[142:143]
; __device__ __forceinline__ void p14_final(Frame& F) {
;     ...
;         { const unsigned char* yr = ys + (size_t)(shbase + t) * DM;
; #pragma unroll
;             for (int j = 0; j < 2; ++j) acc_fp8x16(acc + 16 * j, ldu16(yr + 1024 * j, lb1)); }
;         float* xr = OUTP + (size_t)t * DM; float ss = 0.f;
;         const bf16_t* x1r = WSP(bf16_t, WS_X1) + (size_t)t * DM;
; #pragma unroll
;         for (int j = 0; j < 2; ++j) { const u32x4 xa = ldu16(x1r + 1024 * j, 2u * lb1), xb = ldu16(x1r + 1024 * j + 8, 2u * lb1);
; #pragma unroll
;             for (int q = 0; q < 4; ++q) { const f32x4 g0 = ldf16(gf + 1024 * j + 4 * q, lb4); const u32x4 xw = q < 2 ? xa : xb;
;                 const float a[4] = {bf_lo(xw[(2 * q) & 3]), bf_hi(xw[(2 * q) & 3]), bf_lo(xw[(2 * q + 1) & 3]), bf_hi(xw[(2 * q + 1) & 3])};
; #pragma unroll
;                 for (int i = 0; i < 4; ++i) acc[j * 16 + q * 4 + i] = a[i] + g0[i] * (acc[j * 16 + q * 4 + i] * (1.f / 16.f)); } }
; #pragma unroll
;         for (int i = 0; i < 32; ++i) ss += acc[i] * acc[i];
	v_pk_add_f32 v[44:45], v[44:45], v[144:145]
	v_pk_add_f32 v[46:47], v[46:47], v[146:147]
	v_pk_add_f32 v[0:1], v[0:1], v[78:79]
	v_pk_add_f32 v[54:55], v[48:49], v[148:149]
	v_pk_add_f32 v[56:57], v[50:51], v[150:151]
	v_pk_add_f32 v[66:67], v[52:53], v[152:153]
	v_pk_add_f32 v[2:3], v[2:3], v[80:81]
	v_pk_add_f32 v[42:43], v[42:43], v[154:155]
	v_pk_add_f32 v[36:37], v[36:37], v[156:157]
	v_pk_add_f32 v[34:35], v[34:35], v[158:159]
	v_pk_add_f32 v[32:33], v[32:33], v[82:83]
	v_pk_add_f32 v[30:31], v[30:31], v[160:161]
	v_pk_add_f32 v[28:29], v[28:29], v[162:163]
	v_pk_add_f32 v[26:27], v[26:27], v[164:165]
	v_pk_add_f32 v[38:39], v[38:39], v[84:85]
	v_pk_add_f32 v[40:41], v[40:41], v[166:167]
	v_pk_add_f32 v[44:45], v[44:45], v[168:169]
	v_pk_add_f32 v[46:47], v[46:47], v[170:171]
	v_pk_add_f32 v[48:49], v[0:1], v[86:87]
	v_pk_add_f32 v[50:51], v[54:55], v[172:173]
	v_pk_add_f32 v[52:53], v[56:57], v[174:175]
	v_pk_add_f32 v[54:55], v[66:67], v[176:177]
	v_pk_add_f32 v[56:57], v[2:3], v[88:89]
	v_pk_add_f32 v[42:43], v[42:43], v[178:179]
	v_pk_add_f32 v[36:37], v[36:37], v[180:181]
	v_pk_add_f32 v[34:35], v[34:35], v[182:183]
	v_pk_add_f32 v[32:33], v[32:33], v[90:91]
	v_pk_add_f32 v[30:31], v[30:31], v[184:185]
	v_pk_add_f32 v[28:29], v[28:29], v[186:187]
	v_pk_add_f32 v[26:27], v[26:27], v[188:189]
	v_pk_add_f32 v[38:39], v[38:39], v[92:93]
	s_cbranch_scc0 .LBB0_1766
	s_lshl_b64 s[0:1], s[2:3], 12
	v_lshl_add_u64 v[122:123], v[24:25], 0, s[0:1]
	global_load_dwordx4 v[66:69], v[122:123], off offset:2064
	global_load_dwordx4 v[70:73], v[122:123], off
	global_load_dwordx4 v[74:77], v[122:123], off offset:16
	s_add_i32 s0, s2, s7
	s_ashr_i32 s1, s0, 31
	s_lshl_b64 s[0:1], s[0:1], 11
	v_lshl_add_u64 v[124:125], v[6:7], 0, s[0:1]
	global_load_dwordx4 v[78:81], v[124:125], off
	global_load_dwordx4 v[82:85], v[124:125], off offset:1024
	global_load_dwordx4 v[86:89], v[10:11], off offset:48
	global_load_dwordx4 v[90:93], v[8:9], off
	global_load_dwordx4 v[94:97], v[8:9], off offset:16
	global_load_dwordx4 v[98:101], v[8:9], off offset:32
	global_load_dwordx4 v[102:105], v[8:9], off offset:48
	global_load_dwordx4 v[106:109], v[122:123], off offset:2048
	global_load_dwordx4 v[110:113], v[10:11], off
	global_load_dwordx4 v[114:117], v[10:11], off offset:32
	global_load_dwordx4 v[118:121], v[10:11], off offset:16
	s_waitcnt vmcnt(10)
	v_cvt_pk_f32_fp8_e32 v[132:133], v78
	v_cvt_pk_f32_fp8_sdwa v[134:135], v78 src0_sel:WORD_1
	v_cvt_pk_f32_fp8_e32 v[136:137], v79
	v_cvt_pk_f32_fp8_sdwa v[78:79], v79 src0_sel:WORD_1
	v_cvt_pk_f32_fp8_sdwa v[140:141], v80 src0_sel:WORD_1
	v_cvt_pk_f32_fp8_e32 v[138:139], v80
	v_cvt_pk_f32_fp8_e32 v[142:143], v81
	v_cvt_pk_f32_fp8_sdwa v[80:81], v81 src0_sel:WORD_1
	v_pk_add_f32 v[40:41], v[40:41], v[132:133]
	v_lshlrev_b32_e32 v124, 16, v70
	v_and_b32_e32 v125, 0xffff0000, v70
	v_pk_add_f32 v[44:45], v[44:45], v[134:135]
	v_pk_add_f32 v[48:49], v[48:49], v[78:79]
	v_pk_mul_f32 v[40:41], v[40:41], s[6:7] op_sel_hi:[1,0]
	v_lshlrev_b32_e32 v70, 16, v71
	v_and_b32_e32 v71, 0xffff0000, v71
	v_lshlrev_b32_e32 v126, 16, v72
	v_and_b32_e32 v127, 0xffff0000, v72
	v_lshlrev_b32_e32 v72, 16, v73
	v_and_b32_e32 v73, 0xffff0000, v73
	v_pk_add_f32 v[52:53], v[52:53], v[140:141]
	v_pk_mul_f32 v[44:45], v[44:45], s[6:7] op_sel_hi:[1,0]
	v_pk_mul_f32 v[48:49], v[48:49], s[6:7] op_sel_hi:[1,0]
	s_waitcnt vmcnt(7)
	v_pk_fma_f32 v[40:41], v[40:41], v[90:91], v[124:125]
	v_lshlrev_b32_e32 v128, 16, v74
	v_and_b32_e32 v129, 0xffff0000, v74
	v_lshlrev_b32_e32 v74, 16, v75
	v_and_b32_e32 v75, 0xffff0000, v75
	v_pk_add_f32 v[46:47], v[46:47], v[136:137]
	v_pk_mul_f32 v[52:53], v[52:53], s[6:7] op_sel_hi:[1,0]
	v_pk_fma_f32 v[44:45], v[44:45], v[92:93], v[70:71]
	s_waitcnt vmcnt(6)
	v_pk_fma_f32 v[48:49], v[48:49], v[96:97], v[72:73]
	v_pk_mul_f32 v[72:73], v[40:41], v[40:41]
	v_pk_add_f32 v[56:57], v[56:57], v[80:81]
	v_pk_mul_f32 v[46:47], v[46:47], s[6:7] op_sel_hi:[1,0]
	s_waitcnt vmcnt(5)
	v_pk_fma_f32 v[52:53], v[52:53], v[100:101], v[74:75]
	v_pk_mul_f32 v[74:75], v[44:45], v[44:45]
	v_add_f32_e32 v72, v72, v73
	v_lshlrev_b32_e32 v130, 16, v76
	v_and_b32_e32 v131, 0xffff0000, v76
	v_lshlrev_b32_e32 v76, 16, v77
	v_and_b32_e32 v77, 0xffff0000, v77
	v_pk_mul_f32 v[56:57], v[56:57], s[6:7] op_sel_hi:[1,0]
	v_pk_fma_f32 v[46:47], v[46:47], v[94:95], v[126:127]
	v_add_f32_e32 v72, v74, v72
	v_cvt_pk_f32_fp8_sdwa v[150:151], v85 src0_sel:WORD_1
	s_waitcnt vmcnt(4)
	v_pk_fma_f32 v[56:57], v[56:57], v[104:105], v[76:77]
	v_pk_mul_f32 v[76:77], v[46:47], v[46:47]
	v_add_f32_e32 v72, v75, v72
	v_pk_add_f32 v[50:51], v[50:51], v[138:139]
	v_add_f32_e32 v72, v76, v72
	v_pk_mul_f32 v[50:51], v[50:51], s[6:7] op_sel_hi:[1,0]
	v_pk_mul_f32 v[78:79], v[48:49], v[48:49]
	v_add_f32_e32 v72, v77, v72
	v_pk_fma_f32 v[50:51], v[50:51], v[98:99], v[128:129]
	v_add_f32_e32 v72, v78, v72
	v_pk_add_f32 v[38:39], v[38:39], v[150:151]
	v_pk_mul_f32 v[80:81], v[50:51], v[50:51]
	v_add_f32_e32 v72, v79, v72
	v_and_b32_e32 v123, 0xffff0000, v69
	v_lshlrev_b32_e32 v122, 16, v69
	v_cvt_pk_f32_fp8_e32 v[144:145], v82
	v_pk_add_f32 v[54:55], v[54:55], v[142:143]
	v_pk_mul_f32 v[38:39], v[38:39], s[6:7] op_sel_hi:[1,0]
	v_add_f32_e32 v72, v80, v72
	v_pk_mul_f32 v[54:55], v[54:55], s[6:7] op_sel_hi:[1,0]
	v_pk_fma_f32 v[38:39], v[38:39], v[88:89], v[122:123]
	v_pk_mul_f32 v[88:89], v[52:53], v[52:53]
	v_add_f32_e32 v72, v81, v72
	v_cvt_pk_f32_fp8_sdwa v[146:147], v82 src0_sel:WORD_1
	v_pk_fma_f32 v[54:55], v[54:55], v[102:103], v[130:131]
	v_add_f32_e32 v72, v88, v72
	v_pk_mul_f32 v[90:91], v[54:55], v[54:55]
	v_add_f32_e32 v72, v89, v72
	v_cvt_pk_f32_fp8_e32 v[148:149], v83
	v_pk_add_f32 v[42:43], v[42:43], v[144:145]
	v_add_f32_e32 v72, v90, v72
	v_pk_mul_f32 v[92:93], v[56:57], v[56:57]
	s_waitcnt vmcnt(3)
; __device__ __forceinline__ void p14_final(Frame& F) {
;     ...
;         for (int i = 0; i < 32; ++i) ss += acc[i] * acc[i];
;         const float rstd = 1.f / sqrtf(wave_sum(ss) * (1.f / DM) + EPS_);
; #pragma unroll
;         for (int j = 0; j < 2; ++j)
; #pragma unroll
;             for (int q = 0; q < 4; ++q) { const f32x4 g0 = ldf16(INF(I_FNG) + 1024 * j + 4 * q, lb4); f32x4 o0;
; #pragma unroll
;                 for (int i = 0; i < 4; ++i) o0[i] = acc[j * 16 + q * 4 + i] * rstd * g0[i];
;                 *(f32x4*)((char*)(xr + 1024 * j + 4 * q) + lb4) = o0; }
	v_lshlrev_b32_e32 v94, 16, v106
	v_and_b32_e32 v95, 0xffff0000, v106
	v_pk_mul_f32 v[42:43], v[42:43], s[6:7] op_sel_hi:[1,0]
	v_add_f32_e32 v72, v91, v72
	v_cvt_pk_f32_fp8_sdwa v[82:83], v83 src0_sel:WORD_1
	s_waitcnt vmcnt(2)
	v_pk_fma_f32 v[42:43], v[42:43], v[110:111], v[94:95]
	v_pk_add_f32 v[36:37], v[36:37], v[146:147]
	v_add_f32_e32 v72, v92, v72
	v_pk_mul_f32 v[94:95], v[42:43], v[42:43]
	v_lshlrev_b32_e32 v96, 16, v107
	v_and_b32_e32 v97, 0xffff0000, v107
	v_pk_mul_f32 v[36:37], v[36:37], s[6:7] op_sel_hi:[1,0]
	v_add_f32_e32 v72, v93, v72
	v_cvt_pk_f32_fp8_e32 v[152:153], v84
	v_pk_fma_f32 v[36:37], v[36:37], v[112:113], v[96:97]
	v_pk_add_f32 v[34:35], v[34:35], v[148:149]
	v_add_f32_e32 v72, v94, v72
	v_pk_mul_f32 v[96:97], v[36:37], v[36:37]
	v_lshlrev_b32_e32 v98, 16, v108
	v_and_b32_e32 v99, 0xffff0000, v108
	v_pk_mul_f32 v[34:35], v[34:35], s[6:7] op_sel_hi:[1,0]
	v_add_f32_e32 v72, v95, v72
	v_cvt_pk_f32_fp8_sdwa v[154:155], v84 src0_sel:WORD_1
	s_waitcnt vmcnt(0)
	v_pk_fma_f32 v[34:35], v[34:35], v[118:119], v[98:99]
	v_pk_add_f32 v[32:33], v[32:33], v[82:83]
	v_add_f32_e32 v72, v96, v72
	v_pk_mul_f32 v[98:99], v[34:35], v[34:35]
	v_lshlrev_b32_e32 v82, 16, v109
	v_and_b32_e32 v83, 0xffff0000, v109
	v_pk_mul_f32 v[32:33], v[32:33], s[6:7] op_sel_hi:[1,0]
	v_add_f32_e32 v72, v97, v72
	v_cvt_pk_f32_fp8_e32 v[84:85], v85
	v_pk_fma_f32 v[32:33], v[32:33], v[120:121], v[82:83]
	v_pk_add_f32 v[30:31], v[30:31], v[152:153]
	v_add_f32_e32 v72, v98, v72
	v_pk_mul_f32 v[82:83], v[32:33], v[32:33]
	v_lshlrev_b32_e32 v100, 16, v66
	v_and_b32_e32 v101, 0xffff0000, v66
	v_pk_mul_f32 v[30:31], v[30:31], s[6:7] op_sel_hi:[1,0]
	v_add_f32_e32 v72, v99, v72
	v_pk_fma_f32 v[30:31], v[30:31], v[114:115], v[100:101]
	v_pk_add_f32 v[28:29], v[28:29], v[154:155]
	v_add_f32_e32 v72, v82, v72
	v_pk_mul_f32 v[100:101], v[30:31], v[30:31]
	v_lshlrev_b32_e32 v66, 16, v67
	v_and_b32_e32 v67, 0xffff0000, v67
	v_pk_mul_f32 v[28:29], v[28:29], s[6:7] op_sel_hi:[1,0]
	v_add_f32_e32 v72, v83, v72
	v_pk_fma_f32 v[28:29], v[28:29], v[116:117], v[66:67]
	v_pk_add_f32 v[26:27], v[26:27], v[84:85]
	v_add_f32_e32 v72, v100, v72
	v_pk_mul_f32 v[66:67], v[28:29], v[28:29]
	v_lshlrev_b32_e32 v84, 16, v68
	v_and_b32_e32 v85, 0xffff0000, v68
	v_pk_mul_f32 v[26:27], v[26:27], s[6:7] op_sel_hi:[1,0]
	v_add_f32_e32 v72, v101, v72
	v_pk_fma_f32 v[26:27], v[26:27], v[86:87], v[84:85]
	v_add_f32_e32 v66, v66, v72
	v_pk_mul_f32 v[68:69], v[26:27], v[26:27]
	v_add_f32_e32 v66, v67, v66
	v_add_f32_e32 v66, v68, v66
	v_pk_mul_f32 v[70:71], v[38:39], v[38:39]
	v_add_f32_e32 v66, v69, v66
	v_add_f32_e32 v66, v70, v66
	v_add_f32_e32 v66, v71, v66
	ds_bpermute_b32 v67, v58, v66
	s_waitcnt lgkmcnt(0)
	v_add_f32_e32 v66, v66, v67
	ds_bpermute_b32 v67, v59, v66
	s_waitcnt lgkmcnt(0)
	v_add_f32_e32 v66, v66, v67
	ds_bpermute_b32 v67, v60, v66
	s_waitcnt lgkmcnt(0)
	v_add_f32_e32 v66, v66, v67
	ds_bpermute_b32 v67, v61, v66
	s_waitcnt lgkmcnt(0)
	v_add_f32_e32 v66, v66, v67
	ds_bpermute_b32 v67, v62, v66
	s_waitcnt lgkmcnt(0)
	v_add_f32_e32 v66, v66, v67
	ds_bpermute_b32 v67, v63, v66
	s_waitcnt lgkmcnt(0)
	v_add_f32_e32 v66, v66, v67
	v_fmamk_f32 v66, v66, 0x3a000000, v64
	v_mul_f32_e32 v67, 0x4f800000, v66
	v_cmp_gt_f32_e32 vcc, s12, v66
	s_nop 1
	v_cndmask_b32_e32 v66, v66, v67, vcc
	v_sqrt_f32_e32 v67, v66
	s_nop 0
	v_add_u32_e32 v68, -1, v67
	v_fma_f32 v69, -v68, v67, v66
	v_cmp_ge_f32_e64 s[0:1], 0, v69
	v_add_u32_e32 v69, 1, v67
	s_nop 0
	v_cndmask_b32_e64 v68, v67, v68, s[0:1]
	v_fma_f32 v67, -v69, v67, v66
	v_cmp_lt_f32_e64 s[0:1], 0, v67
	s_nop 1
	v_cndmask_b32_e64 v67, v68, v69, s[0:1]
	v_mul_f32_e32 v68, 0x37800000, v67
	v_cndmask_b32_e32 v67, v67, v68, vcc
	v_cmp_class_f32_e32 vcc, v66, v65
	s_nop 1
	v_cndmask_b32_e32 v68, v67, v66, vcc
	v_div_scale_f32 v69, s[0:1], v68, v68, 1.0
	v_rcp_f32_e32 v70, v69
	s_lshl_b64 s[0:1], s[2:3], 13
	v_lshl_add_u64 v[66:67], v[12:13], 0, s[0:1]
	s_add_i32 s2, s2, s26
	v_fma_f32 v71, -v69, v70, 1.0
	v_fmac_f32_e32 v70, v71, v70
	v_div_scale_f32 v71, vcc, 1.0, v68, 1.0
	v_mul_f32_e32 v72, v71, v70
	v_fma_f32 v73, -v69, v72, v71
	v_fmac_f32_e32 v72, v73, v70
	v_fma_f32 v69, -v69, v72, v71
	v_div_fmas_f32 v69, v69, v70, v72
	v_div_fixup_f32 v68, v69, v68, 1.0
	v_pk_mul_f32 v[40:41], v[40:41], v[68:69] op_sel_hi:[1,0]
	v_pk_mul_f32 v[44:45], v[44:45], v[68:69] op_sel_hi:[1,0]
	v_pk_mul_f32 v[0:1], v[192:193], v[40:41]
	v_pk_mul_f32 v[2:3], v[194:195], v[44:45]
	global_store_dwordx4 v[66:67], v[0:3], off
	v_pk_mul_f32 v[40:41], v[48:49], v[68:69] op_sel_hi:[1,0]
	v_pk_mul_f32 v[44:45], v[46:47], v[68:69] op_sel_hi:[1,0]
	v_pk_mul_f32 v[36:37], v[36:37], v[68:69] op_sel_hi:[1,0]
	v_pk_mul_f32 v[42:43], v[42:43], v[68:69] op_sel_hi:[1,0]
	v_pk_mul_f32 v[32:33], v[32:33], v[68:69] op_sel_hi:[1,0]
	v_pk_mul_f32 v[34:35], v[34:35], v[68:69] op_sel_hi:[1,0]
	v_pk_mul_f32 v[28:29], v[28:29], v[68:69] op_sel_hi:[1,0]
	v_pk_mul_f32 v[30:31], v[30:31], v[68:69] op_sel_hi:[1,0]
	v_pk_mul_f32 v[26:27], v[26:27], v[68:69] op_sel_hi:[1,0]
	s_cmpk_gt_i32 s2, 0x3fff
	v_pk_mul_f32 v[224:225], v[196:197], v[44:45]
	v_pk_mul_f32 v[226:227], v[198:199], v[40:41]
	global_store_dwordx4 v[66:67], v[224:227], off offset:16
	v_pk_mul_f32 v[40:41], v[52:53], v[68:69] op_sel_hi:[1,0]
	v_pk_mul_f32 v[44:45], v[50:51], v[68:69] op_sel_hi:[1,0]
	v_pk_mul_f32 v[2:3], v[202:203], v[40:41]
	v_pk_mul_f32 v[0:1], v[200:201], v[44:45]
	global_store_dwordx4 v[66:67], v[0:3], off offset:32
	v_pk_mul_f32 v[40:41], v[56:57], v[68:69] op_sel_hi:[1,0]
	v_pk_mul_f32 v[44:45], v[54:55], v[68:69] op_sel_hi:[1,0]
	v_pk_mul_f32 v[226:227], v[206:207], v[40:41]
	v_pk_mul_f32 v[224:225], v[204:205], v[44:45]
	global_store_dwordx4 v[66:67], v[224:227], off offset:48
	v_add_co_u32_e32 v40, vcc, s13, v66
	s_nop 0
	v_pk_mul_f32 v[0:1], v[208:209], v[42:43]
	v_addc_co_u32_e32 v41, vcc, 0, v67, vcc
	v_pk_mul_f32 v[2:3], v[210:211], v[36:37]
	global_store_dwordx4 v[40:41], v[0:3], off
	v_pk_mul_f32 v[224:225], v[212:213], v[34:35]
	v_pk_mul_f32 v[226:227], v[214:215], v[32:33]
	global_store_dwordx4 v[40:41], v[224:227], off offset:16
	v_pk_mul_f32 v[0:1], v[216:217], v[30:31]
	v_pk_mul_f32 v[2:3], v[218:219], v[28:29]
	global_store_dwordx4 v[40:41], v[0:3], off offset:32
	v_pk_mul_f32 v[28:29], v[38:39], v[68:69] op_sel_hi:[1,0]
	v_pk_mul_f32 v[224:225], v[220:221], v[26:27]
	v_pk_mul_f32 v[226:227], v[222:223], v[28:29]
	global_store_dwordx4 v[40:41], v[224:227], off offset:48
	s_cbranch_scc0 .LBB0_1765
